# baseline (speedup 1.0000x reference)
_Z4khidPKDF16_PKfS2_S2_S0_PDF16_Pf:
	s_load_dwordx8 s[4:11], s[0:1], 0x0
	s_load_dwordx2 s[12:13], s[0:1], 0x20
	v_lshlrev_b32_e32 v1, 3, v0
	s_lshr_b32 s3, s2, 1
	v_and_b32_e32 v2, 56, v1
	s_and_b32 s15, s3, 0x7ffffffc
	s_lshl_b32 s14, s2, 4
	v_lshlrev_b32_e32 v106, 1, v2
	v_mov_b32_e32 v107, 0
	s_and_b32 s14, s14, 0x70
	v_lshlrev_b32_e32 v126, 2, v2
	s_add_i32 s16, s15, -1
	s_waitcnt lgkmcnt(0)
	v_and_b32_e32 v132, 63, v0
	v_lshlrev_b32_e32 v132, 3, v132
	global_load_dwordx2 v[108:109], v132, s[6:7]
	global_load_dwordx2 v[134:135], v132, s[6:7] offset:512
	global_load_dwordx2 v[136:137], v132, s[6:7] offset:1024
	global_load_dwordx2 v[138:139], v132, s[6:7] offset:1536
	global_load_dwordx4 v[94:97], v126, s[8:9] offset:16
	global_load_dwordx4 v[90:93], v126, s[10:11] offset:16
	global_load_dwordx4 v[102:105], v126, s[8:9]
	global_load_dwordx4 v[98:101], v126, s[10:11]
	v_lshl_add_u64 v[2:3], s[4:5], 0, v[106:107]
	v_mul_u32_u24_e32 v1, 0x1c8, v0
	s_movk_i32 s4, 0xffee
	v_lshrrev_b32_e32 v114, 3, v0
	s_add_i32 s17, s14, -1
	v_mul_i32_i24_sdwa v4, v1, s4 dst_sel:DWORD dst_unused:UNUSED_PAD src0_sel:WORD_1 src1_sel:DWORD
	v_add_u32_sdwa v124, s16, v1 dst_sel:DWORD dst_unused:UNUSED_PAD src0_sel:DWORD src1_sel:WORD_1
	s_movk_i32 s4, 0x7f
	v_add3_u32 v125, s17, v114, v4
	v_med3_i32 v1, v124, 0, s4
	v_med3_i32 v4, v125, 0, s4
	v_lshlrev_b32_e32 v1, 14, v1
	v_or_b32_e32 v121, 32, v114
	v_lshl_or_b32 v106, v4, 7, v1
	v_mul_lo_u16_e32 v1, 57, v121
	v_lshrrev_b16_e32 v1, 10, v1
	v_mul_i32_i24_e32 v6, 0xffffffee, v1
	v_add_u32_e32 v122, s16, v1
	v_add3_u32 v123, s17, v121, v6
	v_min_u32_e32 v1, 0x7f, v122
	v_med3_i32 v6, v123, 0, s4
	v_lshlrev_b32_e32 v1, 14, v1
	v_or_b32_e32 v118, 64, v114
	v_lshl_add_u64 v[4:5], v[2:3], 0, v[106:107]
	v_lshl_or_b32 v106, v6, 7, v1
	v_mul_lo_u16_e32 v1, 57, v118
	v_lshrrev_b16_e32 v1, 10, v1
	v_lshl_add_u64 v[6:7], v[2:3], 0, v[106:107]
	global_load_dwordx4 v[86:89], v[4:5], off
	global_load_dwordx4 v[82:85], v[6:7], off
	v_mul_i32_i24_e32 v4, 0xffffffee, v1
	v_add_u32_e32 v119, s16, v1
	v_add3_u32 v120, s17, v118, v4
	v_min_u32_e32 v1, 0x7f, v119
	v_med3_i32 v4, v120, 0, s4
	v_lshlrev_b32_e32 v1, 14, v1
	v_or_b32_e32 v115, 0x60, v114
	v_lshl_or_b32 v106, v4, 7, v1
	v_mul_lo_u16_e32 v1, 57, v115
	v_lshrrev_b16_e32 v1, 10, v1
	v_mul_i32_i24_e32 v6, 0xffffffee, v1
	v_add_u32_e32 v116, s16, v1
	v_add3_u32 v117, s17, v115, v6
	v_min_u32_e32 v1, 0x7f, v116
	v_med3_i32 v6, v117, 0, s4
	v_lshlrev_b32_e32 v1, 14, v1
	v_lshrrev_b32_e32 v112, 6, v0
	v_lshl_add_u64 v[4:5], v[2:3], 0, v[106:107]
	v_lshl_or_b32 v106, v6, 7, v1
	v_mul_u32_u24_e32 v1, 0x480, v112
	v_and_b32_e32 v113, 63, v0
	v_lshl_add_u64 v[2:3], v[2:3], 0, v[106:107]
	v_lshlrev_b32_e32 v106, 4, v1
	global_load_dwordx4 v[78:81], v[4:5], off
	global_load_dwordx4 v[74:77], v[2:3], off
	v_lshl_add_u64 v[2:3], s[12:13], 0, v[106:107]
	v_lshlrev_b32_e32 v106, 4, v113
	v_lshl_add_u64 v[2:3], v[2:3], 0, v[106:107]
	s_movk_i32 s4, 0x1000
	v_add_co_u32_e32 v4, vcc, s4, v2
	s_movk_i32 s4, 0x2000
	s_nop 0
	v_addc_co_u32_e32 v5, vcc, 0, v3, vcc
	v_add_co_u32_e32 v140, vcc, s4, v2
	s_movk_i32 s4, 0x3000
	s_nop 0
	v_addc_co_u32_e32 v141, vcc, 0, v3, vcc
	v_add_co_u32_e32 v142, vcc, s4, v2
	s_movk_i32 s4, 0x4000
	s_nop 0
	v_addc_co_u32_e32 v143, vcc, 0, v3, vcc
	v_add_co_u32_e32 v110, vcc, s4, v2
	global_load_dwordx4 v[70:73], v[2:3], off
	global_load_dwordx4 v[66:69], v[2:3], off offset:1024
	v_addc_co_u32_e32 v111, vcc, 0, v3, vcc
	global_load_dwordx4 v[62:65], v[2:3], off offset:2048
	global_load_dwordx4 v[58:61], v[2:3], off offset:3072
	global_load_dwordx4 v[50:53], v[4:5], off offset:1024
	global_load_dwordx4 v[46:49], v[4:5], off offset:2048
	global_load_dwordx4 v[42:45], v[4:5], off offset:3072
	global_load_dwordx4 v[18:21], v[142:143], off offset:1024
	global_load_dwordx4 v[14:17], v[142:143], off offset:2048
	global_load_dwordx4 v[10:13], v[142:143], off offset:3072
	global_load_dwordx4 v[54:57], v[140:141], off offset:-4096
	global_load_dwordx4 v[38:41], v[140:141], off
	global_load_dwordx4 v[34:37], v[140:141], off offset:1024
	global_load_dwordx4 v[30:33], v[140:141], off offset:2048
	global_load_dwordx4 v[26:29], v[140:141], off offset:3072
	global_load_dwordx4 v[22:25], v[110:111], off offset:-4096
	global_load_dwordx4 v[6:9], v[110:111], off
	s_nop 0
	global_load_dwordx4 v[2:5], v[110:111], off offset:1024
	v_cmp_eq_u32_e64 s[4:5], 63, v113
	s_waitcnt vmcnt(26)
	v_pk_add_f32 v[108:109], v[108:109], v[134:135]
	v_pk_add_f32 v[136:137], v[136:137], v[138:139]
	v_pk_add_f32 v[108:109], v[108:109], v[136:137]
	s_nop 1
	v_mov_b32_dpp v110, v108 row_shr:1 row_mask:0xf bank_mask:0xf bound_ctrl:1
	v_mov_b32_dpp v111, v109 row_shr:1 row_mask:0xf bank_mask:0xf bound_ctrl:1
	v_pk_add_f32 v[108:109], v[108:109], v[110:111]
	v_lshlrev_b32_e32 v1, 3, v112
	s_nop 0
	v_mov_b32_dpp v110, v108 row_shr:2 row_mask:0xf bank_mask:0xf bound_ctrl:1
	v_mov_b32_dpp v111, v109 row_shr:2 row_mask:0xf bank_mask:0xf bound_ctrl:1
	v_pk_add_f32 v[108:109], v[108:109], v[110:111]
	s_nop 1
	v_mov_b32_dpp v110, v108 row_shr:4 row_mask:0xf bank_mask:0xf bound_ctrl:1
	v_mov_b32_dpp v111, v109 row_shr:4 row_mask:0xf bank_mask:0xf bound_ctrl:1
	v_pk_add_f32 v[108:109], v[108:109], v[110:111]
	s_nop 1
	v_mov_b32_dpp v110, v108 row_shr:8 row_mask:0xf bank_mask:0xf bound_ctrl:1
	v_mov_b32_dpp v111, v109 row_shr:8 row_mask:0xf bank_mask:0xf bound_ctrl:1
	v_pk_add_f32 v[108:109], v[108:109], v[110:111]
	v_mov_b32_e32 v110, v107
	v_mov_b32_e32 v111, v107
	s_nop 0
	v_mov_b32_dpp v110, v108 row_bcast:15 row_mask:0xa bank_mask:0xf
	v_mov_b32_dpp v111, v109 row_bcast:15 row_mask:0xa bank_mask:0xf
	v_pk_add_f32 v[108:109], v[108:109], v[110:111]
	v_mov_b32_e32 v110, 0
	v_mov_b32_e32 v111, 0
	s_nop 0
	v_mov_b32_dpp v110, v108 row_bcast:31 row_mask:0xc bank_mask:0xf
	v_mov_b32_dpp v111, v109 row_bcast:31 row_mask:0xc bank_mask:0xf
	v_pk_add_f32 v[108:109], v[108:109], v[110:111]
	s_mov_b32 s6, 0xf800000
	s_nop 0
	v_readlane_b32 s18, v108, 63
	v_readlane_b32 s19, v109, 63
	s_nop 3
	v_mov_b32_e32 v106, s18
	v_mov_b32_e32 v107, s19
	v_mul_f32_e32 v109, 0x35800000, v106
	v_mul_f32_e32 v106, 0x35800000, v107
	v_fma_f32 v106, -v109, v109, v106
	v_add_f32_e32 v106, 0x3727c5ac, v106
	v_mul_f32_e32 v107, 0x4f800000, v106
	v_cmp_gt_f32_e32 vcc, s6, v106
	s_nop 1
	v_cndmask_b32_e32 v106, v106, v107, vcc
	v_sqrt_f32_e32 v107, v106
	s_nop 0
	v_add_u32_e32 v108, -1, v107
	v_fma_f32 v110, -v108, v107, v106
	v_cmp_ge_f32_e64 s[6:7], 0, v110
	v_add_u32_e32 v110, 1, v107
	s_nop 0
	v_cndmask_b32_e64 v108, v107, v108, s[6:7]
	v_fma_f32 v107, -v110, v107, v106
	v_cmp_lt_f32_e64 s[6:7], 0, v107
	s_nop 1
	v_cndmask_b32_e64 v107, v108, v110, s[6:7]
	v_mul_f32_e32 v108, 0x37800000, v107
	v_cndmask_b32_e32 v107, v107, v108, vcc
	v_mov_b32_e32 v108, 0x260
	v_cmp_class_f32_e32 vcc, v106, v108
	s_nop 1
	v_cndmask_b32_e32 v106, v107, v106, vcc
	v_div_scale_f32 v107, s[6:7], v106, v106, 1.0
	v_rcp_f32_e32 v108, v107
	s_movk_i32 s6, 0x360
	v_cmp_gt_u32_e64 s[6:7], s6, v0
	v_fma_f32 v110, -v107, v108, 1.0
	v_fmac_f32_e32 v108, v110, v108
	v_div_scale_f32 v110, vcc, 1.0, v106, 1.0
	v_mul_f32_e32 v111, v110, v108
	v_fma_f32 v126, -v107, v111, v110
	v_fmac_f32_e32 v111, v126, v108
	v_fma_f32 v107, -v107, v111, v110
	v_div_fmas_f32 v107, v107, v108, v111
	v_div_fixup_f32 v110, v107, v106, 1.0
	s_waitcnt vmcnt(22)
	v_mul_f32_e32 v102, v110, v102
	v_mul_f32_e32 v94, v110, v94
	s_waitcnt vmcnt(22)
	v_fma_f32 v106, -v109, v102, v98
	v_fma_f32 v98, -v109, v94, v90
	v_mul_f32_e32 v107, v110, v103
	v_mul_f32_e32 v95, v110, v95
	v_xor_b32_e32 v90, v114, v0
	v_fma_f32 v108, -v109, v107, v99
	v_fma_f32 v99, -v109, v95, v91
	v_mul_f32_e32 v103, v110, v104
	v_mul_f32_e32 v91, v110, v96
	v_mul_f32_e32 v104, v110, v105
	v_mul_f32_e32 v96, v110, v97
	v_lshlrev_b32_e32 v90, 4, v90
	v_fma_f32 v100, -v109, v103, v100
	v_fma_f32 v92, -v109, v91, v92
	v_fma_f32 v97, -v109, v104, v101
	v_fma_f32 v93, -v109, v96, v93
	v_and_b32_e32 v90, 0x70, v90
	s_waitcnt vmcnt(18)
	v_fma_mixlo_f16 v101, v86, v102, v106 op_sel_hi:[1,0,0]
	v_fma_mixhi_f16 v101, v86, v107, v108 op_sel:[1,0,0] op_sel_hi:[1,0,0]
	v_pk_max_f16 v101, v101, 0
	v_fma_mixlo_f16 v86, v87, v103, v100 op_sel_hi:[1,0,0]
	v_fma_mixhi_f16 v86, v87, v104, v97 op_sel:[1,0,0] op_sel_hi:[1,0,0]
	v_pk_max_f16 v86, v86, 0
	v_fma_mixlo_f16 v87, v88, v94, v98 op_sel_hi:[1,0,0]
	v_fma_mixhi_f16 v87, v88, v95, v99 op_sel:[1,0,0] op_sel_hi:[1,0,0]
	v_pk_max_f16 v87, v87, 0
	v_fma_mixlo_f16 v88, v89, v91, v92 op_sel_hi:[1,0,0]
	v_fma_mixhi_f16 v88, v89, v96, v93 op_sel:[1,0,0] op_sel_hi:[1,0,0]
	v_pk_max_f16 v88, v88, 0
	s_and_saveexec_b64 s[8:9], s[6:7]
	s_cbranch_execz .LBB1_4
	v_or_b32_e32 v89, v125, v124
	s_movk_i32 s6, 0x80
	v_cmp_gt_u32_e32 vcc, s6, v89
	v_lshl_or_b32 v105, v114, 7, v90
	s_nop 0
	v_cndmask_b32_e32 v89, 0, v88, vcc
	v_cndmask_b32_e32 v88, 0, v87, vcc
	v_cndmask_b32_e32 v87, 0, v86, vcc
	v_cndmask_b32_e32 v86, 0, v101, vcc
	ds_write_b128 v105, v[86:89]

.LBB1_10:
	s_or_b64 exec, exec, s[8:9]
	v_lshrrev_b32_e32 v75, 4, v113
	v_and_b32_e32 v74, 15, v0
	v_lshlrev_b32_e32 v92, 7, v74
	v_bitop3_b32 v76, v0, v75, 7 bitop3:0x6c
	v_lshl_or_b32 v108, v76, 4, v92
	s_waitcnt lgkmcnt(0)
	s_barrier
	ds_read_b128 v[76:79], v108
	v_add_u32_e32 v96, 18, v74
	v_add_u32_e32 v100, 36, v74
	v_lshlrev_b32_e32 v97, 7, v96
	v_bitop3_b32 v80, v96, v75, 7 bitop3:0x6c
	v_lshlrev_b32_e32 v101, 7, v100
	v_bitop3_b32 v84, v100, v75, 7 bitop3:0x6c
	v_lshl_or_b32 v109, v80, 4, v97
	v_lshl_or_b32 v110, v84, 4, v101
	v_add_u32_e32 v104, 54, v74
	v_or_b32_e32 v113, 4, v75
	v_add_u32_e32 v118, 1, v74
	ds_read_b128 v[80:83], v109
	ds_read_b128 v[84:87], v110
	v_lshlrev_b32_e32 v105, 7, v104
	v_bitop3_b32 v88, v104, v75, 7 bitop3:0x6c
	v_bitop3_b32 v93, v0, v113, 7 bitop3:0x6c
	v_bitop3_b32 v96, v96, v113, 7 bitop3:0x6c
	v_bitop3_b32 v100, v100, v113, 7 bitop3:0x6c
	v_bitop3_b32 v104, v104, v113, 7 bitop3:0x6c
	v_lshlrev_b32_e32 v119, 7, v118
	v_bitop3_b32 v120, v118, v75, 7 bitop3:0x6c
	v_lshl_or_b32 v111, v88, 4, v105
	v_lshl_or_b32 v114, v93, 4, v92
	v_lshl_or_b32 v115, v96, 4, v97
	v_lshl_or_b32 v116, v100, 4, v101
	v_lshl_or_b32 v117, v104, 4, v105
	v_lshl_or_b32 v120, v120, 4, v119
	ds_read_b128 v[88:91], v111
	ds_read_b128 v[92:95], v114
	ds_read_b128 v[96:99], v115
	ds_read_b128 v[100:103], v116
	ds_read_b128 v[104:107], v117
	s_waitcnt lgkmcnt(7)
	s_waitcnt vmcnt(0)
	v_mfma_f32_16x16x32_f16 a[0:3], v[70:73], v[76:79], 0
	ds_read_b128 v[76:79], v120
	v_add_u32_e32 v120, 19, v74
	v_lshlrev_b32_e32 v121, 7, v120
	v_bitop3_b32 v122, v120, v75, 7 bitop3:0x6c
	v_lshl_or_b32 v122, v122, 4, v121
	v_add_u32_e32 v123, 37, v74
	v_add_u32_e32 v126, 55, v74
	s_waitcnt lgkmcnt(7)
	v_mfma_f32_16x16x32_f16 a[4:7], v[70:73], v[80:83], 0
	ds_read_b128 v[80:83], v122
	v_lshlrev_b32_e32 v124, 7, v123
	v_bitop3_b32 v125, v123, v75, 7 bitop3:0x6c
	s_waitcnt lgkmcnt(7)
	v_mfma_f32_16x16x32_f16 a[8:11], v[70:73], v[84:87], 0
	v_lshlrev_b32_e32 v127, 7, v126
	v_bitop3_b32 v128, v126, v75, 7 bitop3:0x6c
	v_lshl_or_b32 v125, v125, 4, v124
	v_lshl_or_b32 v128, v128, 4, v127
	ds_read_b128 v[84:87], v125
	s_waitcnt lgkmcnt(7)
	v_mfma_f32_16x16x32_f16 a[12:15], v[70:73], v[88:91], 0
	ds_read_b128 v[70:73], v128
	v_bitop3_b32 v88, v118, v113, 7 bitop3:0x6c
	v_lshl_or_b32 v88, v88, 4, v119
	s_waitcnt lgkmcnt(7)
	v_mfma_f32_16x16x32_f16 a[0:3], v[66:69], v[92:95], a[0:3]
	v_bitop3_b32 v92, v120, v113, 7 bitop3:0x6c
	v_lshl_or_b32 v118, v92, 4, v121
	ds_read_b128 v[88:91], v88
	s_waitcnt lgkmcnt(7)
	v_mfma_f32_16x16x32_f16 a[4:7], v[66:69], v[96:99], a[4:7]
	ds_read_b128 v[92:95], v118
	v_bitop3_b32 v96, v123, v113, 7 bitop3:0x6c
	v_lshl_or_b32 v119, v96, 4, v124
	s_waitcnt lgkmcnt(7)
	v_mfma_f32_16x16x32_f16 a[8:11], v[66:69], v[100:103], a[8:11]
	v_add_u32_e32 v101, 2, v74
	v_bitop3_b32 v100, v126, v113, 7 bitop3:0x6c
	v_lshlrev_b32_e32 v102, 7, v101
	v_bitop3_b32 v103, v101, v75, 7 bitop3:0x6c
	v_lshl_or_b32 v100, v100, 4, v127
	v_lshl_or_b32 v103, v103, 4, v102
	ds_read_b128 v[96:99], v119
	s_waitcnt lgkmcnt(7)
	v_mfma_f32_16x16x32_f16 a[12:15], v[66:69], v[104:107], a[12:15]
	ds_read_b128 v[66:69], v100
	v_add_u32_e32 v106, 38, v74
	v_lshlrev_b32_e32 v107, 7, v106
	s_waitcnt lgkmcnt(7)
	v_mfma_f32_16x16x32_f16 a[0:3], v[62:65], v[76:79], a[0:3]
	ds_read_b128 v[76:79], v103
	v_add_u32_e32 v103, 20, v74
	v_lshlrev_b32_e32 v104, 7, v103
	v_bitop3_b32 v105, v103, v75, 7 bitop3:0x6c
	v_lshl_or_b32 v105, v105, 4, v104
	s_waitcnt lgkmcnt(7)
	v_mfma_f32_16x16x32_f16 a[4:7], v[62:65], v[80:83], a[4:7]
	ds_read_b128 v[80:83], v105
	s_lshl_b32 s3, s3, 7
	s_or_b32 s3, s3, 0x180
	s_waitcnt lgkmcnt(7)
	v_mfma_f32_16x16x32_f16 a[8:11], v[62:65], v[84:87], a[8:11]
	v_bitop3_b32 v84, v106, v75, 7 bitop3:0x6c
	v_lshl_or_b32 v120, v84, 4, v107
	ds_read_b128 v[84:87], v120
	s_waitcnt lgkmcnt(7)
	v_mfma_f32_16x16x32_f16 a[12:15], v[62:65], v[70:73], a[12:15]
	v_bitop3_b32 v70, v101, v113, 7 bitop3:0x6c
	ds_read_b128 v[62:65], v108 offset:7168
	v_lshl_or_b32 v70, v70, 4, v102
	s_waitcnt lgkmcnt(7)
	v_mfma_f32_16x16x32_f16 a[0:3], v[58:61], v[88:91], a[0:3]
	v_bitop3_b32 v88, v103, v113, 7 bitop3:0x6c
	ds_read_b128 v[70:73], v70
	v_lshl_or_b32 v101, v88, 4, v104
	s_waitcnt lgkmcnt(7)
	v_mfma_f32_16x16x32_f16 a[4:7], v[58:61], v[92:95], a[4:7]
	v_bitop3_b32 v92, v106, v113, 7 bitop3:0x6c
	ds_read_b128 v[88:91], v101
	s_waitcnt lgkmcnt(7)
	v_mfma_f32_16x16x32_f16 a[8:11], v[58:61], v[96:99], a[8:11]
	v_lshl_or_b32 v96, v92, 4, v107
	ds_read_b128 v[92:95], v96
	s_waitcnt lgkmcnt(7)
	v_mfma_f32_16x16x32_f16 a[12:15], v[58:61], v[66:69], a[12:15]
	ds_read_b128 v[58:61], v114 offset:7168
	s_waitcnt lgkmcnt(7)
	v_mfma_f32_16x16x32_f16 a[0:3], v[54:57], v[76:79], a[0:3]
	ds_read_b128 v[66:69], v109
	s_waitcnt lgkmcnt(7)
	v_mfma_f32_16x16x32_f16 a[4:7], v[54:57], v[80:83], a[4:7]
	ds_read_b128 v[76:79], v110
	s_waitcnt lgkmcnt(7)
	v_mfma_f32_16x16x32_f16 a[8:11], v[54:57], v[84:87], a[8:11]
	ds_read_b128 v[80:83], v111
	s_waitcnt lgkmcnt(7)
	v_mfma_f32_16x16x32_f16 a[12:15], v[54:57], v[62:65], a[12:15]
	ds_read_b128 v[54:57], v108 offset:9216
	s_waitcnt lgkmcnt(7)
	v_mfma_f32_16x16x32_f16 a[0:3], v[50:53], v[70:73], a[0:3]
	ds_read_b128 v[62:65], v115
	s_waitcnt lgkmcnt(7)
	v_mfma_f32_16x16x32_f16 a[4:7], v[50:53], v[88:91], a[4:7]
	ds_read_b128 v[70:73], v116
	s_waitcnt lgkmcnt(7)
	v_mfma_f32_16x16x32_f16 a[8:11], v[50:53], v[92:95], a[8:11]
	ds_read_b128 v[84:87], v117
	s_waitcnt lgkmcnt(7)
	v_mfma_f32_16x16x32_f16 a[12:15], v[50:53], v[58:61], a[12:15]
	ds_read_b128 v[50:53], v114 offset:9216
	s_waitcnt lgkmcnt(7)
	v_mfma_f32_16x16x32_f16 a[0:3], v[46:49], v[66:69], a[0:3]
	ds_read_b128 v[58:61], v122
	s_waitcnt lgkmcnt(7)
	v_mfma_f32_16x16x32_f16 a[4:7], v[46:49], v[76:79], a[4:7]
	ds_read_b128 v[66:69], v125
	s_waitcnt lgkmcnt(7)
	v_mfma_f32_16x16x32_f16 a[8:11], v[46:49], v[80:83], a[8:11]
	v_add_u32_e32 v80, 0x49, v74
	ds_read_b128 v[76:79], v128
	v_lshlrev_b32_e32 v81, 7, v80
	s_waitcnt lgkmcnt(7)
	v_mfma_f32_16x16x32_f16 a[12:15], v[46:49], v[54:57], a[12:15]
	v_bitop3_b32 v46, v80, v75, 7 bitop3:0x6c
	v_lshl_or_b32 v82, v46, 4, v81
	ds_read_b128 v[46:49], v82
	s_waitcnt lgkmcnt(7)
	v_mfma_f32_16x16x32_f16 a[0:3], v[42:45], v[62:65], a[0:3]
	ds_read_b128 v[54:57], v118
	s_waitcnt lgkmcnt(7)
	v_mfma_f32_16x16x32_f16 a[4:7], v[42:45], v[70:73], a[4:7]
	ds_read_b128 v[62:65], v119
	s_waitcnt lgkmcnt(7)
	v_mfma_f32_16x16x32_f16 a[8:11], v[42:45], v[84:87], a[8:11]
	ds_read_b128 v[70:73], v100
	s_waitcnt lgkmcnt(7)
	v_mfma_f32_16x16x32_f16 a[12:15], v[42:45], v[50:53], a[12:15]
	v_bitop3_b32 v42, v80, v113, 7 bitop3:0x6c
	v_lshl_or_b32 v80, v42, 4, v81
	ds_read_b128 v[42:45], v80
	s_waitcnt lgkmcnt(7)
	v_mfma_f32_16x16x32_f16 a[0:3], v[38:41], v[58:61], a[0:3]
	ds_read_b128 v[50:53], v105
	s_waitcnt lgkmcnt(7)
	v_mfma_f32_16x16x32_f16 a[4:7], v[38:41], v[66:69], a[4:7]
	ds_read_b128 v[58:61], v120
	s_waitcnt lgkmcnt(7)
	v_mfma_f32_16x16x32_f16 a[8:11], v[38:41], v[76:79], a[8:11]
	v_add_u32_e32 v76, 0x4a, v74
	ds_read_b128 v[66:69], v108 offset:7168
	v_lshlrev_b32_e32 v77, 7, v76
	s_waitcnt lgkmcnt(7)
	v_mfma_f32_16x16x32_f16 a[12:15], v[38:41], v[46:49], a[12:15]
	v_bitop3_b32 v38, v76, v75, 7 bitop3:0x6c
	v_lshl_or_b32 v78, v38, 4, v77
	ds_read_b128 v[38:41], v78
	s_waitcnt lgkmcnt(7)
	v_mfma_f32_16x16x32_f16 a[0:3], v[34:37], v[54:57], a[0:3]
	ds_read_b128 v[46:49], v101
	s_waitcnt lgkmcnt(7)
	v_mfma_f32_16x16x32_f16 a[4:7], v[34:37], v[62:65], a[4:7]
	ds_read_b128 v[54:57], v96
	s_waitcnt lgkmcnt(7)
	v_mfma_f32_16x16x32_f16 a[8:11], v[34:37], v[70:73], a[8:11]
	ds_read_b128 v[62:65], v114 offset:7168
	s_waitcnt lgkmcnt(7)
	v_mfma_f32_16x16x32_f16 a[12:15], v[34:37], v[42:45], a[12:15]
	v_bitop3_b32 v34, v76, v113, 7 bitop3:0x6c
	v_lshl_or_b32 v70, v34, 4, v77
	ds_read_b128 v[34:37], v70
	s_waitcnt lgkmcnt(7)
	v_mfma_f32_16x16x32_f16 a[0:3], v[30:33], v[50:53], a[0:3]
	ds_read_b128 v[42:45], v110
	s_waitcnt lgkmcnt(7)
	v_mfma_f32_16x16x32_f16 a[4:7], v[30:33], v[58:61], a[4:7]
	ds_read_b128 v[50:53], v111
	s_waitcnt lgkmcnt(7)
	v_mfma_f32_16x16x32_f16 a[8:11], v[30:33], v[66:69], a[8:11]
	v_add_u32_e32 v66, 0x5a, v74
	ds_read_b128 v[58:61], v108 offset:9216
	v_lshlrev_b32_e32 v67, 7, v66
	s_waitcnt lgkmcnt(7)
	v_mfma_f32_16x16x32_f16 a[12:15], v[30:33], v[38:41], a[12:15]
	v_bitop3_b32 v30, v66, v75, 7 bitop3:0x6c
	v_lshl_or_b32 v30, v30, 4, v67
	ds_read_b128 v[30:33], v30
	s_waitcnt lgkmcnt(7)
	v_mfma_f32_16x16x32_f16 a[0:3], v[26:29], v[46:49], a[0:3]
	ds_read_b128 v[38:41], v116
	s_waitcnt lgkmcnt(7)
	v_mfma_f32_16x16x32_f16 a[4:7], v[26:29], v[54:57], a[4:7]
	ds_read_b128 v[46:49], v117
	s_waitcnt lgkmcnt(7)
	v_mfma_f32_16x16x32_f16 a[8:11], v[26:29], v[62:65], a[8:11]
	ds_read_b128 v[54:57], v114 offset:9216
	s_waitcnt lgkmcnt(7)
	v_mfma_f32_16x16x32_f16 a[12:15], v[26:29], v[34:37], a[12:15]
	v_bitop3_b32 v26, v66, v113, 7 bitop3:0x6c
	v_lshl_or_b32 v26, v26, 4, v67
	ds_read_b128 v[26:29], v26
	s_waitcnt lgkmcnt(7)
	v_mfma_f32_16x16x32_f16 a[0:3], v[22:25], v[42:45], a[0:3]
	ds_read_b128 v[34:37], v125
	s_waitcnt lgkmcnt(7)
	v_mfma_f32_16x16x32_f16 a[4:7], v[22:25], v[50:53], a[4:7]
	ds_read_b128 v[42:45], v128
	s_waitcnt lgkmcnt(7)
	v_mfma_f32_16x16x32_f16 a[8:11], v[22:25], v[58:61], a[8:11]
	v_add_u32_e32 v58, 0x5b, v74
	ds_read_b128 v[50:53], v82
	v_lshlrev_b32_e32 v59, 7, v58
	s_waitcnt lgkmcnt(7)
	v_mfma_f32_16x16x32_f16 a[12:15], v[22:25], v[30:33], a[12:15]
	v_bitop3_b32 v22, v58, v75, 7 bitop3:0x6c
	v_lshl_or_b32 v22, v22, 4, v59
	ds_read_b128 v[22:25], v22
	s_waitcnt lgkmcnt(7)
	v_mfma_f32_16x16x32_f16 a[0:3], v[18:21], v[38:41], a[0:3]
	ds_read_b128 v[30:33], v119
	s_waitcnt lgkmcnt(7)
	v_mfma_f32_16x16x32_f16 a[4:7], v[18:21], v[46:49], a[4:7]
	ds_read_b128 v[38:41], v100
	s_waitcnt lgkmcnt(7)
	v_mfma_f32_16x16x32_f16 a[8:11], v[18:21], v[54:57], a[8:11]
	ds_read_b128 v[46:49], v80
	s_waitcnt lgkmcnt(7)
	v_mfma_f32_16x16x32_f16 a[12:15], v[18:21], v[26:29], a[12:15]
	v_bitop3_b32 v18, v58, v113, 7 bitop3:0x6c
	v_lshl_or_b32 v18, v18, 4, v59
	ds_read_b128 v[18:21], v18
	s_waitcnt lgkmcnt(7)
	v_mfma_f32_16x16x32_f16 a[0:3], v[14:17], v[34:37], a[0:3]
	ds_read_b128 v[26:29], v120
	s_waitcnt lgkmcnt(7)
	v_mfma_f32_16x16x32_f16 a[4:7], v[14:17], v[42:45], a[4:7]
	ds_read_b128 v[34:37], v108 offset:7168
	s_waitcnt lgkmcnt(7)
	v_mfma_f32_16x16x32_f16 a[8:11], v[14:17], v[50:53], a[8:11]
	v_add_u32_e32 v50, 0x5c, v74
	ds_read_b128 v[42:45], v78
	v_lshlrev_b32_e32 v51, 7, v50
	s_waitcnt lgkmcnt(7)
	v_mfma_f32_16x16x32_f16 a[12:15], v[14:17], v[22:25], a[12:15]
	v_bitop3_b32 v14, v50, v75, 7 bitop3:0x6c
	v_lshl_or_b32 v14, v14, 4, v51
	ds_read_b128 v[14:17], v14
	s_waitcnt lgkmcnt(7)
	v_mfma_f32_16x16x32_f16 a[0:3], v[10:13], v[30:33], a[0:3]
	ds_read_b128 v[22:25], v96
	s_waitcnt lgkmcnt(7)
	v_mfma_f32_16x16x32_f16 a[4:7], v[10:13], v[38:41], a[4:7]
	ds_read_b128 v[30:33], v114 offset:7168
	s_waitcnt lgkmcnt(7)
	v_mfma_f32_16x16x32_f16 a[8:11], v[10:13], v[46:49], a[8:11]
	ds_read_b128 v[38:41], v70
	s_waitcnt lgkmcnt(7)
	v_mfma_f32_16x16x32_f16 a[12:15], v[10:13], v[18:21], a[12:15]
	v_bitop3_b32 v10, v50, v113, 7 bitop3:0x6c
	v_lshl_or_b32 v10, v10, 4, v51
	ds_read_b128 v[10:13], v10
	s_waitcnt lgkmcnt(7)
	v_mfma_f32_16x16x32_f16 a[0:3], v[6:9], v[26:29], a[0:3]
	v_lshl_or_b32 v26, s15, 7, v74
	s_waitcnt lgkmcnt(6)
	v_mfma_f32_16x16x32_f16 a[4:7], v[6:9], v[34:37], a[4:7]
	s_waitcnt lgkmcnt(5)
	v_mfma_f32_16x16x32_f16 a[8:11], v[6:9], v[42:45], a[8:11]
	s_waitcnt lgkmcnt(4)
	v_mfma_f32_16x16x32_f16 a[12:15], v[6:9], v[14:17], a[12:15]
	s_waitcnt lgkmcnt(3)
	v_mfma_f32_16x16x32_f16 a[0:3], v[2:5], v[22:25], a[0:3]
	s_nop 7
	v_accvgpr_read_b32 v6, a0
	v_accvgpr_read_b32 v20, a1
	v_accvgpr_read_b32 v21, a2
	v_accvgpr_read_b32 v7, a3
	s_waitcnt lgkmcnt(2)
	v_mfma_f32_16x16x32_f16 a[0:3], v[2:5], v[30:33], a[4:7]
	v_mul_f32_e32 v24, v20, v20
	v_fmac_f32_e32 v24, v6, v6
	v_fmac_f32_e32 v24, v21, v21
	s_nop 4
	v_accvgpr_read_b32 v14, a2
	v_accvgpr_read_b32 v15, a3
	s_waitcnt lgkmcnt(1)
	v_mfma_f32_16x16x32_f16 a[2:5], v[2:5], v[38:41], a[8:11]
	v_accvgpr_read_b32 v8, a0
	v_accvgpr_read_b32 v9, a1
	s_nop 5
	v_accvgpr_read_b32 v18, a4
	v_accvgpr_read_b32 v19, a5
	s_waitcnt lgkmcnt(0)
	v_mfma_f32_16x16x32_f16 a[4:7], v[2:5], v[10:13], a[12:15]
	v_lshlrev_b32_e32 v2, 5, v112
	v_mov_b32_e32 v3, 0
	v_lshl_add_u64 v[12:13], s[6:7], 0, v[2:3]
	v_lshlrev_b32_e32 v2, 3, v75
	v_lshl_add_u64 v[12:13], v[12:13], 0, v[2:3]
	v_add_f32_e32 v2, 0, v6
	v_add_f32_e32 v2, v2, v20
	v_add_f32_e32 v2, v2, v21
	v_add_f32_e32 v25, v2, v7
	v_or_b32_e32 v2, s14, v26
	v_lshlrev_b64 v[22:23], 7, v[2:3]
	v_cvt_pk_f16_f32 v21, v21, v7
	v_cvt_pk_f16_f32 v20, v6, v20
	v_lshl_add_u64 v[22:23], v[12:13], 0, v[22:23]
	v_pk_mov_b32 v[6:7], v[6:7], v[8:9] op_sel:[1,0]
	global_store_dwordx2 v[22:23], v[20:21], off
	v_accvgpr_read_b32 v21, a1
	v_pk_mul_f32 v[6:7], v[6:7], v[6:7]
	v_add_f32_e32 v2, v25, v8
	v_accvgpr_read_b32 v20, a0
	v_add_f32_e32 v6, v24, v6
	v_add_f32_e32 v22, v6, v7
	v_add_f32_e32 v2, v2, v9
	v_pk_mul_f32 v[6:7], v[14:15], v[14:15]
	v_pk_mul_f32 v[20:21], v[20:21], v[20:21]
	v_add_f32_e32 v2, v2, v14
	v_add_f32_e32 v7, v22, v21
	v_add_u32_e32 v22, s14, v26
	v_add_f32_e32 v21, v2, v15
	v_add_u32_e32 v2, 0x80, v22
	v_add_f32_e32 v20, v7, v6
	v_cvt_pk_f16_f32 v6, v8, v9
	v_lshlrev_b64 v[8:9], 7, v[2:3]
	v_accvgpr_read_b32 v16, a2
	v_accvgpr_read_b32 v17, a3
	v_cvt_pk_f16_f32 v7, v14, v15
	v_lshl_add_u64 v[8:9], v[12:13], 0, v[8:9]
	global_store_dwordx2 v[8:9], v[6:7], off
	v_add_f32_e32 v2, v21, v16
	v_pk_mov_b32 v[6:7], v[14:15], v[16:17] op_sel:[1,0]
	v_accvgpr_read_b32 v9, a3
	v_pk_mul_f32 v[6:7], v[6:7], v[6:7]
	v_add_f32_e32 v2, v2, v17
	v_accvgpr_read_b32 v8, a2
	v_add_f32_e32 v6, v20, v6
	v_add_f32_e32 v2, v2, v18
	v_add_f32_e32 v14, v6, v7
	v_pk_mul_f32 v[6:7], v[18:19], v[18:19]
	v_pk_mul_f32 v[8:9], v[8:9], v[8:9]
	v_add_f32_e32 v15, v2, v19
	v_add_u32_e32 v2, 0x100, v22
	v_add_f32_e32 v7, v14, v9
	v_lshlrev_b64 v[8:9], 7, v[2:3]
	v_accvgpr_read_b32 v4, a4
	v_accvgpr_read_b32 v5, a5
	v_add_f32_e32 v14, v7, v6
	v_cvt_pk_f16_f32 v7, v18, v19
	v_cvt_pk_f16_f32 v6, v16, v17
	v_lshl_add_u64 v[8:9], v[12:13], 0, v[8:9]
	global_store_dwordx2 v[8:9], v[6:7], off
	v_pk_mov_b32 v[6:7], v[18:19], v[4:5] op_sel:[1,0]
	v_accvgpr_read_b32 v9, a5
	v_pk_mul_f32 v[6:7], v[6:7], v[6:7]
	v_add_f32_e32 v2, v15, v4
	v_accvgpr_read_b32 v8, a4
	v_add_f32_e32 v6, v14, v6
	v_accvgpr_read_b32 v10, a6
	v_accvgpr_read_b32 v11, a7
	v_add_f32_e32 v7, v6, v7
	v_add_f32_e32 v2, v2, v5
	v_pk_mul_f32 v[8:9], v[8:9], v[8:9]
	v_add_f32_e32 v6, v2, v10
	v_pk_mul_f32 v[14:15], v[10:11], v[10:11]
	v_add_f32_e32 v2, v7, v9
	v_add_f32_e32 v9, v2, v14
	v_or_b32_e32 v2, s3, v74
	v_or_b32_e32 v2, s14, v2
	v_cvt_pk_f16_f32 v14, v4, v5
	v_lshlrev_b64 v[4:5], 7, v[2:3]
	v_mul_f32_e32 v7, v11, v11
	v_cvt_pk_f16_f32 v15, v10, v11
	v_lshl_add_u64 v[4:5], v[12:13], 0, v[4:5]
	v_accvgpr_read_b32 v8, a7
	global_store_dwordx2 v[4:5], v[14:15], off
	v_pk_add_f32 v[4:5], v[6:7], v[8:9]
	v_mov_b32_e32 v2, v3
	s_nop 0
	v_mov_b32_dpp v6, v4 row_shr:1 row_mask:0xf bank_mask:0xf bound_ctrl:1
	v_mov_b32_dpp v7, v5 row_shr:1 row_mask:0xf bank_mask:0xf bound_ctrl:1
	v_pk_add_f32 v[4:5], v[4:5], v[6:7]
	s_nop 1
	v_mov_b32_dpp v6, v4 row_shr:2 row_mask:0xf bank_mask:0xf bound_ctrl:1
	v_mov_b32_dpp v7, v5 row_shr:2 row_mask:0xf bank_mask:0xf bound_ctrl:1
	v_pk_add_f32 v[4:5], v[4:5], v[6:7]
	s_nop 1
	v_mov_b32_dpp v6, v4 row_shr:4 row_mask:0xf bank_mask:0xf bound_ctrl:1
	v_mov_b32_dpp v7, v5 row_shr:4 row_mask:0xf bank_mask:0xf bound_ctrl:1
	v_pk_add_f32 v[4:5], v[4:5], v[6:7]
	s_nop 1
	v_mov_b32_dpp v6, v4 row_shr:8 row_mask:0xf bank_mask:0xf bound_ctrl:1
	v_mov_b32_dpp v7, v5 row_shr:8 row_mask:0xf bank_mask:0xf bound_ctrl:1
	v_pk_add_f32 v[4:5], v[4:5], v[6:7]
	v_mov_b32_e32 v6, v3
	v_mov_b32_e32 v7, v3
	s_nop 0
	v_mov_b32_dpp v6, v4 row_bcast:15 row_mask:0xa bank_mask:0xf
	v_mov_b32_dpp v7, v5 row_bcast:15 row_mask:0xa bank_mask:0xf
	v_pk_add_f32 v[4:5], v[4:5], v[6:7]
	s_nop 1
	v_mov_b32_dpp v2, v4 row_bcast:31 row_mask:0xc bank_mask:0xf
	v_mov_b32_dpp v3, v5 row_bcast:31 row_mask:0xc bank_mask:0xf
	s_and_saveexec_b64 s[6:7], s[4:5]
	v_pk_add_f32 v[2:3], v[4:5], v[2:3]
	ds_write_b64 v1, v[2:3] offset:14080
	s_or_b64 exec, exec, s[6:7]
	v_cmp_eq_u32_e32 vcc, 0, v0
	s_waitcnt lgkmcnt(0)
	s_barrier
	s_and_saveexec_b64 s[4:5], vcc
	s_cbranch_execz .LBB1_14
	v_mov_b32_e32 v8, 0
	s_load_dwordx2 s[0:1], s[0:1], 0x30
	ds_read_b128 v[0:3], v8 offset:14080
	ds_read_b128 v[4:7], v8 offset:14096
	s_lshl_b32 s2, s2, 1
	s_mov_b32 s3, 0
	s_lshl_b64 s[2:3], s[2:3], 2
	s_waitcnt lgkmcnt(0)
	v_pk_add_f32 v[0:1], v[0:1], v[2:3]
	s_add_u32 s0, s0, s2
	v_pk_add_f32 v[0:1], v[0:1], v[4:5]
	s_addc_u32 s1, s1, s3
	v_pk_add_f32 v[0:1], v[0:1], v[6:7]
	global_store_dwordx2 v8, v[0:1], s[0:1]

	.amdhsa_kernel _Z4khidPKDF16_PKfS2_S2_S0_PDF16_Pf
		.amdhsa_group_segment_fixed_size 14112
		.amdhsa_private_segment_fixed_size 0
		.amdhsa_kernarg_size 56
		.amdhsa_user_sgpr_count 2
		.amdhsa_user_sgpr_dispatch_ptr 0
		.amdhsa_user_sgpr_queue_ptr 0
		.amdhsa_user_sgpr_kernarg_segment_ptr 1
		.amdhsa_user_sgpr_dispatch_id 0
		.amdhsa_user_sgpr_kernarg_preload_length 0
		.amdhsa_user_sgpr_kernarg_preload_offset 0
		.amdhsa_user_sgpr_private_segment_size 0
		.amdhsa_uses_dynamic_stack 0
		.amdhsa_enable_private_segment 0
		.amdhsa_system_sgpr_workgroup_id_x 1
		.amdhsa_system_sgpr_workgroup_id_y 0
		.amdhsa_system_sgpr_workgroup_id_z 0
		.amdhsa_system_sgpr_workgroup_info 0
		.amdhsa_system_vgpr_workitem_id 0
		.amdhsa_next_free_vgpr 160
		.amdhsa_next_free_sgpr 20
		.amdhsa_accum_offset 144
		.amdhsa_reserve_vcc 1
		.amdhsa_float_round_mode_32 0
		.amdhsa_float_round_mode_16_64 0
		.amdhsa_float_denorm_mode_32 3
		.amdhsa_float_denorm_mode_16_64 3
		.amdhsa_dx10_clamp 1
		.amdhsa_ieee_mode 1
		.amdhsa_fp16_overflow 0
		.amdhsa_tg_split 0
		.amdhsa_exception_fp_ieee_invalid_op 0
		.amdhsa_exception_fp_denorm_src 0
		.amdhsa_exception_fp_ieee_div_zero 0
		.amdhsa_exception_fp_ieee_overflow 0
		.amdhsa_exception_fp_ieee_underflow 0
		.amdhsa_exception_fp_ieee_inexact 0
		.amdhsa_exception_int_div_zero 0
	.end_amdhsa_kernel

amdhsa.kernels:
  - .agpr_count:     0
    .args:
      - .actual_access:  read_only
        .address_space:  global
        .offset:         0
        .size:           8
        .value_kind:     global_buffer
      - .actual_access:  read_only
        .address_space:  global
        .offset:         8
        .size:           8
        .value_kind:     global_buffer
      - .actual_access:  read_only
        .address_space:  global
        .offset:         16
        .size:           8
        .value_kind:     global_buffer
      - .actual_access:  read_only
        .address_space:  global
        .offset:         24
        .size:           8
        .value_kind:     global_buffer
      - .actual_access:  read_only
        .address_space:  global
        .offset:         32
        .size:           8
        .value_kind:     global_buffer
      - .actual_access:  read_only
        .address_space:  global
        .offset:         40
        .size:           8
        .value_kind:     global_buffer
      - .actual_access:  write_only
        .address_space:  global
        .offset:         48
        .size:           8
        .value_kind:     global_buffer
      - .actual_access:  write_only
        .address_space:  global
        .offset:         56
        .size:           8
        .value_kind:     global_buffer
      - .actual_access:  write_only
        .address_space:  global
        .offset:         64
        .size:           8
        .value_kind:     global_buffer
      - .actual_access:  write_only
        .address_space:  global
        .offset:         72
        .size:           8
        .value_kind:     global_buffer
    .group_segment_fixed_size: 12000
    .kernarg_segment_align: 8
    .kernarg_segment_size: 80
    .language:       OpenCL C
    .language_version:
      - 2
      - 0
    .max_flat_workgroup_size: 256
    .name:           _Z2k0PKfS0_S0_S0_S0_S0_PDF16_PfS1_S1_
    .private_segment_fixed_size: 0
    .sgpr_count:     24
    .sgpr_spill_count: 0
    .symbol:         _Z2k0PKfS0_S0_S0_S0_S0_PDF16_PfS1_S1_.kd
    .uniform_work_group_size: 1
    .uses_dynamic_stack: false
    .vgpr_count:     150
    .vgpr_spill_count: 0
    .wavefront_size: 64
  - .agpr_count:     16
    .args:
      - .actual_access:  read_only
        .address_space:  global
        .offset:         0
        .size:           8
        .value_kind:     global_buffer
      - .actual_access:  read_only
        .address_space:  global
        .offset:         8
        .size:           8
        .value_kind:     global_buffer
      - .actual_access:  read_only
        .address_space:  global
        .offset:         16
        .size:           8
        .value_kind:     global_buffer
      - .actual_access:  read_only
        .address_space:  global
        .offset:         24
        .size:           8
        .value_kind:     global_buffer
      - .actual_access:  read_only
        .address_space:  global
        .offset:         32
        .size:           8
        .value_kind:     global_buffer
      - .actual_access:  write_only
        .address_space:  global
        .offset:         40
        .size:           8
        .value_kind:     global_buffer
      - .actual_access:  write_only
        .address_space:  global
        .offset:         48
        .size:           8
        .value_kind:     global_buffer
    .group_segment_fixed_size: 14112
    .kernarg_segment_align: 8
    .kernarg_segment_size: 56
    .language:       OpenCL C
    .language_version:
      - 2
      - 0
    .max_flat_workgroup_size: 256
    .name:           _Z4khidPKDF16_PKfS2_S2_S0_PDF16_Pf
    .private_segment_fixed_size: 0
    .sgpr_count:     26
    .sgpr_spill_count: 0
    .symbol:         _Z4khidPKDF16_PKfS2_S2_S0_PDF16_Pf.kd
    .uniform_work_group_size: 1
    .uses_dynamic_stack: false
    .vgpr_count:     160
    .vgpr_spill_count: 0
    .wavefront_size: 64
  - .agpr_count:     144
    .args:
      - .actual_access:  read_only
        .address_space:  global
        .offset:         0
        .size:           8
        .value_kind:     global_buffer
      - .actual_access:  read_only
        .address_space:  global
        .offset:         8
        .size:           8
        .value_kind:     global_buffer
      - .actual_access:  read_only
        .address_space:  global
        .offset:         16
        .size:           8
        .value_kind:     global_buffer
      - .actual_access:  read_only
        .address_space:  global
        .offset:         24
        .size:           8
        .value_kind:     global_buffer
      - .address_space:  global
        .offset:         32
        .size:           8
        .value_kind:     global_buffer
      - .address_space:  global
        .offset:         40
        .size:           8
        .value_kind:     global_buffer
      - .address_space:  global
        .offset:         48
        .size:           8
        .value_kind:     global_buffer
    .group_segment_fixed_size: 0
    .kernarg_segment_align: 8
    .kernarg_segment_size: 56
    .language:       OpenCL C
    .language_version:
      - 2
      - 0
    .max_flat_workgroup_size: 256
    .name:           _Z6kfinalPKDF16_PKfS2_S2_PK15HIP_vector_typeIjLj4EES2_Pf
    .private_segment_fixed_size: 0
    .sgpr_count:     41
    .sgpr_spill_count: 0
    .symbol:         _Z6kfinalPKDF16_PKfS2_S2_PK15HIP_vector_typeIjLj4EES2_Pf.kd
    .uniform_work_group_size: 1
    .uses_dynamic_stack: false
    .vgpr_count:     400
    .vgpr_spill_count: 0
    .wavefront_size: 64
  - .agpr_count:     73
    .args:
      - .actual_access:  read_only
        .address_space:  global
        .offset:         0
        .size:           8
        .value_kind:     global_buffer
      - .actual_access:  read_only
        .address_space:  global
        .offset:         8
        .size:           8
        .value_kind:     global_buffer
      - .actual_access:  read_only
        .address_space:  global
        .offset:         16
        .size:           8
        .value_kind:     global_buffer
      - .actual_access:  read_only
        .address_space:  global
        .offset:         24
        .size:           8
        .value_kind:     global_buffer
      - .address_space:  global
        .offset:         32
        .size:           8
        .value_kind:     global_buffer
      - .address_space:  global
        .offset:         40
        .size:           8
        .value_kind:     global_buffer
      - .address_space:  global
        .offset:         48
        .size:           8
        .value_kind:     global_buffer
    .group_segment_fixed_size: 0
    .kernarg_segment_align: 8
    .kernarg_segment_size: 56
    .language:       OpenCL C
    .language_version:
      - 2
      - 0
    .max_flat_workgroup_size: 512
    .name:           _Z7kfinal3PKDF16_PKfS2_S2_PK15HIP_vector_typeIjLj4EES2_Pf
    .private_segment_fixed_size: 0
    .sgpr_count:     60
    .sgpr_spill_count: 0
    .symbol:         _Z7kfinal3PKDF16_PKfS2_S2_PK15HIP_vector_typeIjLj4EES2_Pf.kd
    .uniform_work_group_size: 1
    .uses_dynamic_stack: false
    .vgpr_count:     253
    .vgpr_spill_count: 0
    .wavefront_size: 64
